# v105 + first K-loop iteration peeled in the k0, k3, k9 and k10 GEMM copies: its first MFMA into each accumulator quad takes 0 as addend, so the 128-register zeroing before the loop is deleted
# speedup vs baseline: 1.0052x; 1.0052x over previous
.LBB0_199:
	s_add_u32 s8, s34, 0x40080
	s_addc_u32 s9, s35, 0
	s_add_u32 s67, s38, 0x100
	v_mov_b32_e32 v10, 0
	v_lshl_add_u64 v[224:225], s[8:9], 0, v[220:221]
	v_lshl_add_u64 v[226:227], s[8:9], 0, v[222:223]
	s_addc_u32 s68, s39, 0
	s_mov_b32 s69, -2
	s_mov_b64 s[38:39], 0
	s_xor_b64 s[40:41], s[36:37], -1
	v_add_u32_e32 v66, 0, v219
	v_add_u32_e32 v140, 0x10000, v66
	v_add_u32_e32 v66, 0x14000, v66
	ds_read_b128 v[156:159], v140
	ds_read_b128 v[160:163], v140 offset:1024
	ds_read_b128 v[164:167], v140 offset:2048
	ds_read_b128 v[168:171], v140 offset:3072
	ds_read_b128 v[140:143], v66
	ds_read_b128 v[144:147], v66 offset:1024
	ds_read_b128 v[148:151], v66 offset:2048
	ds_read_b128 v[152:155], v66 offset:3072
	s_cmp_lg_u32 s38, 0
	s_cselect_b64 s[8:9], -1, 0
	s_mov_b64 s[26:27], -1
	s_or_b64 s[64:65], s[40:41], s[8:9]
	v_lshl_add_u64 v[228:229], v[224:225], 0, s[38:39]
	s_add_i32 m0, s85, 0xc000
	ds_read_b128 v[196:199], v244
	ds_read_b128 v[200:203], v244 offset:1024
	ds_read_b128 v[188:191], v244 offset:2048
	ds_read_b128 v[192:195], v244 offset:3072
	ds_read_b128 v[180:183], v244 offset:4096
	ds_read_b128 v[184:187], v244 offset:5120
	ds_read_b128 v[172:175], v244 offset:6144
	ds_read_b128 v[176:179], v244 offset:7168
	global_load_lds_dwordx4 v[228:229], off
	v_lshl_add_u64 v[228:229], v[226:227], 0, s[38:39]
	s_add_i32 m0, s85, 0xe000
	s_and_b64 vcc, exec, s[64:65]
	global_load_lds_dwordx4 v[228:229], off
	s_cbranch_vccz .Lpeelk0_203
	s_waitcnt vmcnt(8)
	s_mov_b64 s[26:27], 0

.Lpeelk0_205:
	s_add_u32 s8, s34, s38
	s_addc_u32 s9, s35, s39
	s_add_u32 s8, s8, 0x100
	s_addc_u32 s9, s9, 0
	s_add_u32 s10, s67, s38
	s_addc_u32 s11, s68, s39
	s_waitcnt lgkmcnt(0)
	s_cmpk_eq_i32 s38, 0x700
	s_cselect_b32 s59, s55, s9
	s_cselect_b32 s58, s54, s8
	s_cselect_b32 s37, s57, s11
	s_cselect_b32 s36, s56, s10
	s_barrier
	s_setprio 1
	s_waitcnt lgkmcnt(0)
	v_mfma_f32_16x16x32_bf16 v[136:139], v[156:159], v[196:199], 0
	v_mfma_f32_16x16x32_bf16 v[132:135], v[164:167], v[196:199], 0
	v_mfma_f32_16x16x32_bf16 v[120:123], v[156:159], v[188:191], 0
	v_mfma_f32_16x16x32_bf16 v[116:119], v[164:167], v[188:191], 0
	v_mfma_f32_16x16x32_bf16 v[104:107], v[156:159], v[180:183], 0
	v_mfma_f32_16x16x32_bf16 v[100:103], v[164:167], v[180:183], 0
	v_mfma_f32_16x16x32_bf16 v[88:91], v[156:159], v[172:175], 0
	v_mfma_f32_16x16x32_bf16 v[84:87], v[164:167], v[172:175], 0
	v_mfma_f32_16x16x32_bf16 v[136:139], v[160:163], v[200:203], v[136:139]
	v_mfma_f32_16x16x32_bf16 v[132:135], v[168:171], v[200:203], v[132:135]
	v_mfma_f32_16x16x32_bf16 v[120:123], v[160:163], v[192:195], v[120:123]
	v_mfma_f32_16x16x32_bf16 v[116:119], v[168:171], v[192:195], v[116:119]
	v_mfma_f32_16x16x32_bf16 v[104:107], v[160:163], v[184:187], v[104:107]
	v_mfma_f32_16x16x32_bf16 v[100:103], v[168:171], v[184:187], v[100:103]
	v_mfma_f32_16x16x32_bf16 v[88:91], v[160:163], v[176:179], v[88:91]
	v_mfma_f32_16x16x32_bf16 v[84:87], v[168:171], v[176:179], v[84:87]
	s_setprio 0
	s_setprio 1
	v_mfma_f32_16x16x32_bf16 v[128:131], v[140:143], v[196:199], 0
	v_mfma_f32_16x16x32_bf16 v[124:127], v[148:151], v[196:199], 0
	v_mfma_f32_16x16x32_bf16 v[112:115], v[140:143], v[188:191], 0
	v_mfma_f32_16x16x32_bf16 v[108:111], v[148:151], v[188:191], 0
	v_mfma_f32_16x16x32_bf16 v[96:99], v[140:143], v[180:183], 0
	v_mfma_f32_16x16x32_bf16 v[92:95], v[148:151], v[180:183], 0
	v_mfma_f32_16x16x32_bf16 v[80:83], v[140:143], v[172:175], 0
	v_mfma_f32_16x16x32_bf16 v[76:79], v[148:151], v[172:175], 0
	v_mfma_f32_16x16x32_bf16 v[128:131], v[144:147], v[200:203], v[128:131]
	v_mfma_f32_16x16x32_bf16 v[124:127], v[152:155], v[200:203], v[124:127]
	v_mfma_f32_16x16x32_bf16 v[112:115], v[144:147], v[192:195], v[112:115]
	v_mfma_f32_16x16x32_bf16 v[108:111], v[152:155], v[192:195], v[108:111]
	v_mfma_f32_16x16x32_bf16 v[96:99], v[144:147], v[184:187], v[96:99]
	v_mfma_f32_16x16x32_bf16 v[92:95], v[152:155], v[184:187], v[92:95]
	v_mfma_f32_16x16x32_bf16 v[80:83], v[144:147], v[176:179], v[80:83]
	v_mfma_f32_16x16x32_bf16 v[76:79], v[152:155], v[176:179], v[76:79]
	s_setprio 0
	s_barrier
	s_mov_b32 m0, s86
	v_lshl_add_u64 v[234:235], s[36:37], 0, v[210:211]
	s_add_u32 s8, s36, 0x40000
	ds_read_b128 v[196:199], v244 offset:16384
	ds_read_b128 v[200:203], v244 offset:17408
	ds_read_b128 v[188:191], v244 offset:18432
	ds_read_b128 v[192:195], v244 offset:19456
	ds_read_b128 v[180:183], v244 offset:20480
	ds_read_b128 v[184:187], v244 offset:21504
	ds_read_b128 v[172:175], v244 offset:22528
	ds_read_b128 v[176:179], v244 offset:23552
	global_load_lds_dwordx4 v[234:235], off
	v_lshl_add_u64 v[232:233], s[36:37], 0, v[214:215]
	s_mov_b32 m0, s87
	s_addc_u32 s9, s37, 0
	global_load_lds_dwordx4 v[232:233], off
	v_lshl_add_u64 v[228:229], s[8:9], 0, v[210:211]
	s_mov_b32 m0, s88
	v_lshl_add_u64 v[230:231], s[58:59], 0, v[212:213]
	global_load_lds_dwordx4 v[228:229], off
	v_lshl_add_u64 v[228:229], s[8:9], 0, v[214:215]
	s_mov_b32 m0, s89
	s_mov_b64 s[26:27], -1
	global_load_lds_dwordx4 v[228:229], off
	v_lshl_add_u64 v[228:229], s[58:59], 0, v[208:209]
	s_mov_b32 m0, s85
	s_and_b64 vcc, exec, s[64:65]
	global_load_lds_dwordx4 v[228:229], off
	s_mov_b32 m0, s90
	s_nop 0
	global_load_lds_dwordx4 v[230:231], off
	s_cbranch_vccz .Lpeelk0_207
	s_waitcnt vmcnt(8)
	s_mov_b64 s[26:27], 0

.Lpeelk0_T:
	s_waitcnt lgkmcnt(0)
	s_barrier
	s_setprio 1
	s_waitcnt lgkmcnt(0)
	v_mfma_f32_16x16x32_bf16 v[72:75], v[156:159], v[196:199], 0
	v_mfma_f32_16x16x32_bf16 v[68:71], v[164:167], v[196:199], 0
	v_mfma_f32_16x16x32_bf16 v[54:57], v[156:159], v[188:191], 0
	v_mfma_f32_16x16x32_bf16 v[50:53], v[164:167], v[188:191], 0
	v_mfma_f32_16x16x32_bf16 v[38:41], v[156:159], v[180:183], 0
	v_mfma_f32_16x16x32_bf16 v[34:37], v[164:167], v[180:183], 0
	v_mfma_f32_16x16x32_bf16 v[22:25], v[156:159], v[172:175], 0
	v_mfma_f32_16x16x32_bf16 v[18:21], v[164:167], v[172:175], 0
	v_mfma_f32_16x16x32_bf16 v[72:75], v[160:163], v[200:203], v[72:75]
	v_mfma_f32_16x16x32_bf16 v[68:71], v[168:171], v[200:203], v[68:71]
	v_mfma_f32_16x16x32_bf16 v[54:57], v[160:163], v[192:195], v[54:57]
	v_mfma_f32_16x16x32_bf16 v[50:53], v[168:171], v[192:195], v[50:53]
	v_mfma_f32_16x16x32_bf16 v[38:41], v[160:163], v[184:187], v[38:41]
	v_mfma_f32_16x16x32_bf16 v[34:37], v[168:171], v[184:187], v[34:37]
	v_mfma_f32_16x16x32_bf16 v[22:25], v[160:163], v[176:179], v[22:25]
	v_mfma_f32_16x16x32_bf16 v[18:21], v[168:171], v[176:179], v[18:21]
	s_setprio 0
	s_setprio 1
	v_mfma_f32_16x16x32_bf16 v[62:65], v[140:143], v[196:199], 0
	v_mfma_f32_16x16x32_bf16 v[58:61], v[148:151], v[196:199], 0
	v_mfma_f32_16x16x32_bf16 v[46:49], v[140:143], v[188:191], 0
	v_mfma_f32_16x16x32_bf16 v[42:45], v[148:151], v[188:191], 0
	v_mfma_f32_16x16x32_bf16 v[30:33], v[140:143], v[180:183], 0
	v_mfma_f32_16x16x32_bf16 v[26:29], v[148:151], v[180:183], 0
	v_mfma_f32_16x16x32_bf16 v[14:17], v[140:143], v[172:175], 0
	v_mfma_f32_16x16x32_bf16 v[10:13], v[148:151], v[172:175], 0
	v_mfma_f32_16x16x32_bf16 v[62:65], v[144:147], v[200:203], v[62:65]
	v_mfma_f32_16x16x32_bf16 v[58:61], v[152:155], v[200:203], v[58:61]
	v_mfma_f32_16x16x32_bf16 v[46:49], v[144:147], v[192:195], v[46:49]
	v_mfma_f32_16x16x32_bf16 v[42:45], v[152:155], v[192:195], v[42:45]
	v_mfma_f32_16x16x32_bf16 v[30:33], v[144:147], v[184:187], v[30:33]
	v_mfma_f32_16x16x32_bf16 v[26:29], v[152:155], v[184:187], v[26:29]
	v_mfma_f32_16x16x32_bf16 v[14:17], v[144:147], v[176:179], v[14:17]
	v_mfma_f32_16x16x32_bf16 v[10:13], v[152:155], v[176:179], v[10:13]
	s_setprio 0
	s_barrier
	s_add_i32 s10, 0, 0x18000
	v_add_u32_e32 v66, s10, v219
	s_add_i32 s11, 0, 0x1c000
	ds_read_b128 v[140:143], v66
	ds_read_b128 v[144:147], v66 offset:1024
	ds_read_b128 v[148:151], v66 offset:2048
	ds_read_b128 v[152:155], v66 offset:3072
	v_add_u32_e32 v66, s11, v219
	ds_read_b128 v[156:159], v66
	ds_read_b128 v[160:163], v66 offset:1024
	ds_read_b128 v[164:167], v66 offset:2048
	ds_read_b128 v[168:171], v66 offset:3072
	s_add_u32 s8, s58, 0x40000
	s_addc_u32 s9, s59, 0
	s_mov_b32 m0, s91
	v_lshl_add_u64 v[246:247], s[8:9], 0, v[208:209]
	ds_read_b128 v[172:175], v244 offset:32768
	ds_read_b128 v[176:179], v244 offset:33792
	ds_read_b128 v[180:183], v244 offset:34816
	ds_read_b128 v[184:187], v244 offset:35840
	ds_read_b128 v[188:191], v244 offset:36864
	ds_read_b128 v[192:195], v244 offset:37888
	ds_read_b128 v[196:199], v244 offset:38912
	ds_read_b128 v[200:203], v244 offset:39936
	global_load_lds_dwordx4 v[246:247], off
	v_lshl_add_u64 v[246:247], s[8:9], 0, v[212:213]
	s_mov_b32 m0, s92
	s_nop 0
	global_load_lds_dwordx4 v[246:247], off
	s_waitcnt vmcnt(8)
	s_waitcnt lgkmcnt(0)
	s_barrier
	s_setprio 1
	s_waitcnt lgkmcnt(0)
	v_mfma_f32_16x16x32_bf16 v[136:139], v[140:143], v[172:175], v[136:139]
	v_mfma_f32_16x16x32_bf16 v[132:135], v[148:151], v[172:175], v[132:135]
	v_mfma_f32_16x16x32_bf16 v[120:123], v[140:143], v[180:183], v[120:123]
	v_mfma_f32_16x16x32_bf16 v[116:119], v[148:151], v[180:183], v[116:119]
	v_mfma_f32_16x16x32_bf16 v[104:107], v[140:143], v[188:191], v[104:107]
	v_mfma_f32_16x16x32_bf16 v[100:103], v[148:151], v[188:191], v[100:103]
	v_mfma_f32_16x16x32_bf16 v[88:91], v[140:143], v[196:199], v[88:91]
	v_mfma_f32_16x16x32_bf16 v[84:87], v[148:151], v[196:199], v[84:87]
	v_mfma_f32_16x16x32_bf16 v[136:139], v[144:147], v[176:179], v[136:139]
	v_mfma_f32_16x16x32_bf16 v[132:135], v[152:155], v[176:179], v[132:135]
	v_mfma_f32_16x16x32_bf16 v[120:123], v[144:147], v[184:187], v[120:123]
	v_mfma_f32_16x16x32_bf16 v[116:119], v[152:155], v[184:187], v[116:119]
	v_mfma_f32_16x16x32_bf16 v[104:107], v[144:147], v[192:195], v[104:107]
	v_mfma_f32_16x16x32_bf16 v[100:103], v[152:155], v[192:195], v[100:103]
	v_mfma_f32_16x16x32_bf16 v[88:91], v[144:147], v[200:203], v[88:91]
	v_mfma_f32_16x16x32_bf16 v[84:87], v[152:155], v[200:203], v[84:87]
	s_setprio 0
	s_setprio 1
	v_mfma_f32_16x16x32_bf16 v[128:131], v[156:159], v[172:175], v[128:131]
	v_mfma_f32_16x16x32_bf16 v[124:127], v[164:167], v[172:175], v[124:127]
	v_mfma_f32_16x16x32_bf16 v[112:115], v[156:159], v[180:183], v[112:115]
	v_mfma_f32_16x16x32_bf16 v[108:111], v[164:167], v[180:183], v[108:111]
	v_mfma_f32_16x16x32_bf16 v[96:99], v[156:159], v[188:191], v[96:99]
	v_mfma_f32_16x16x32_bf16 v[92:95], v[164:167], v[188:191], v[92:95]
	v_mfma_f32_16x16x32_bf16 v[80:83], v[156:159], v[196:199], v[80:83]
	v_mfma_f32_16x16x32_bf16 v[76:79], v[164:167], v[196:199], v[76:79]
	v_mfma_f32_16x16x32_bf16 v[128:131], v[160:163], v[176:179], v[128:131]
	v_mfma_f32_16x16x32_bf16 v[124:127], v[168:171], v[176:179], v[124:127]
	v_mfma_f32_16x16x32_bf16 v[112:115], v[160:163], v[184:187], v[112:115]
	v_mfma_f32_16x16x32_bf16 v[108:111], v[168:171], v[184:187], v[108:111]
	v_mfma_f32_16x16x32_bf16 v[96:99], v[160:163], v[192:195], v[96:99]
	v_mfma_f32_16x16x32_bf16 v[92:95], v[168:171], v[192:195], v[92:95]
	v_mfma_f32_16x16x32_bf16 v[80:83], v[160:163], v[200:203], v[80:83]
	v_mfma_f32_16x16x32_bf16 v[76:79], v[168:171], v[200:203], v[76:79]
	s_setprio 0
	s_barrier
	s_add_i32 s8, s10, s84
	v_lshl_add_u64 v[234:235], v[234:235], 0, s[60:61]
	s_mov_b32 m0, s8
	ds_read_b128 v[172:175], v244 offset:49152
	ds_read_b128 v[176:179], v244 offset:50176
	ds_read_b128 v[180:183], v244 offset:51200
	ds_read_b128 v[184:187], v244 offset:52224
	ds_read_b128 v[188:191], v244 offset:53248
	ds_read_b128 v[192:195], v244 offset:54272
	ds_read_b128 v[196:199], v244 offset:55296
	ds_read_b128 v[200:203], v244 offset:56320
	global_load_lds_dwordx4 v[234:235], off
	s_add_i32 m0, s8, 0x2000
	s_add_u32 s8, s36, 0x40080
	v_lshl_add_u64 v[232:233], v[232:233], 0, s[60:61]
	s_addc_u32 s9, s37, 0
	s_add_i32 s10, s11, s84
	global_load_lds_dwordx4 v[232:233], off
	v_lshl_add_u64 v[232:233], s[8:9], 0, v[210:211]
	s_mov_b32 m0, s10
	v_lshl_add_u64 v[228:229], v[228:229], 0, s[60:61]
	global_load_lds_dwordx4 v[232:233], off
	v_lshl_add_u64 v[232:233], s[8:9], 0, v[214:215]
	s_add_i32 m0, s10, 0x2000
	s_nop 0
	global_load_lds_dwordx4 v[232:233], off
	s_mov_b32 m0, s96
	s_nop 0
	global_load_lds_dwordx4 v[228:229], off
	v_lshl_add_u64 v[228:229], v[230:231], 0, s[60:61]
	s_mov_b32 m0, s97
	s_nop 0
	global_load_lds_dwordx4 v[228:229], off
	s_waitcnt vmcnt(8)
	s_waitcnt lgkmcnt(0)
	s_barrier
	s_setprio 1
	s_waitcnt lgkmcnt(0)
	v_mfma_f32_16x16x32_bf16 v[72:75], v[140:143], v[172:175], v[72:75]
	v_mfma_f32_16x16x32_bf16 v[68:71], v[148:151], v[172:175], v[68:71]
	v_mfma_f32_16x16x32_bf16 v[54:57], v[140:143], v[180:183], v[54:57]
	v_mfma_f32_16x16x32_bf16 v[50:53], v[148:151], v[180:183], v[50:53]
	v_mfma_f32_16x16x32_bf16 v[38:41], v[140:143], v[188:191], v[38:41]
	v_mfma_f32_16x16x32_bf16 v[34:37], v[148:151], v[188:191], v[34:37]
	v_mfma_f32_16x16x32_bf16 v[22:25], v[140:143], v[196:199], v[22:25]
	v_mfma_f32_16x16x32_bf16 v[18:21], v[148:151], v[196:199], v[18:21]
	v_mfma_f32_16x16x32_bf16 v[72:75], v[144:147], v[176:179], v[72:75]
	v_mfma_f32_16x16x32_bf16 v[68:71], v[152:155], v[176:179], v[68:71]
	v_mfma_f32_16x16x32_bf16 v[54:57], v[144:147], v[184:187], v[54:57]
	v_mfma_f32_16x16x32_bf16 v[50:53], v[152:155], v[184:187], v[50:53]
	v_mfma_f32_16x16x32_bf16 v[38:41], v[144:147], v[192:195], v[38:41]
	v_mfma_f32_16x16x32_bf16 v[34:37], v[152:155], v[192:195], v[34:37]
	v_mfma_f32_16x16x32_bf16 v[22:25], v[144:147], v[200:203], v[22:25]
	v_mfma_f32_16x16x32_bf16 v[18:21], v[152:155], v[200:203], v[18:21]
	s_setprio 0
	s_setprio 1
	v_mfma_f32_16x16x32_bf16 v[62:65], v[156:159], v[172:175], v[62:65]
	v_mfma_f32_16x16x32_bf16 v[58:61], v[164:167], v[172:175], v[58:61]
	v_mfma_f32_16x16x32_bf16 v[46:49], v[156:159], v[180:183], v[46:49]
	v_mfma_f32_16x16x32_bf16 v[42:45], v[164:167], v[180:183], v[42:45]
	v_mfma_f32_16x16x32_bf16 v[30:33], v[156:159], v[188:191], v[30:33]
	v_mfma_f32_16x16x32_bf16 v[26:29], v[164:167], v[188:191], v[26:29]
	v_mfma_f32_16x16x32_bf16 v[14:17], v[156:159], v[196:199], v[14:17]
	v_mfma_f32_16x16x32_bf16 v[10:13], v[164:167], v[196:199], v[10:13]
	v_mfma_f32_16x16x32_bf16 v[62:65], v[160:163], v[176:179], v[62:65]
	v_mfma_f32_16x16x32_bf16 v[58:61], v[168:171], v[176:179], v[58:61]
	v_mfma_f32_16x16x32_bf16 v[46:49], v[160:163], v[184:187], v[46:49]
	v_mfma_f32_16x16x32_bf16 v[42:45], v[168:171], v[184:187], v[42:45]
	v_mfma_f32_16x16x32_bf16 v[30:33], v[160:163], v[192:195], v[30:33]
	v_mfma_f32_16x16x32_bf16 v[26:29], v[168:171], v[192:195], v[26:29]
	v_mfma_f32_16x16x32_bf16 v[14:17], v[160:163], v[200:203], v[14:17]
	v_mfma_f32_16x16x32_bf16 v[10:13], v[168:171], v[200:203], v[10:13]
	s_setprio 0
	s_barrier
	s_add_i32 s69, s69, 2
	s_add_u32 s38, s38, 0x100
	s_addc_u32 s39, s39, 0
	s_cmp_gt_u32 s69, 13
	s_cbranch_scc1 .LBB0_209
	s_branch .LBB0_201

.LBB0_798:
	s_add_u32 s8, s40, 0x100080
	s_addc_u32 s9, s41, 0
	s_add_u32 s70, s36, 0x100
	v_mov_b32_e32 v2, 0
	v_lshl_add_u64 v[212:213], s[8:9], 0, v[208:209]
	v_lshl_add_u64 v[214:215], s[8:9], 0, v[210:211]
	s_addc_u32 s71, s37, 0
	s_mov_b32 s8, -2
	s_mov_b64 s[58:59], 0
	s_xor_b64 s[64:65], s[64:65], -1
	v_add_u32_e32 v132, 0, v225
	v_add_u32_e32 v133, 0x10000, v132
	v_add_u32_e32 v144, 0x14000, v132
	ds_read_b128 v[148:151], v133
	ds_read_b128 v[152:155], v133 offset:1024
	ds_read_b128 v[156:159], v133 offset:2048
	ds_read_b128 v[160:163], v133 offset:3072
	ds_read_b128 v[132:135], v144
	ds_read_b128 v[136:139], v144 offset:1024
	ds_read_b128 v[140:143], v144 offset:2048
	ds_read_b128 v[144:147], v144 offset:3072
	s_cmp_lg_u32 s58, 0
	s_cselect_b64 s[10:11], -1, 0
	s_mov_b64 s[26:27], -1
	s_or_b64 s[68:69], s[64:65], s[10:11]
	v_lshl_add_u64 v[216:217], v[212:213], 0, s[58:59]
	s_add_i32 m0, s74, 0xc000
	ds_read_b128 v[188:191], v226
	ds_read_b128 v[192:195], v226 offset:1024
	ds_read_b128 v[180:183], v226 offset:2048
	ds_read_b128 v[184:187], v226 offset:3072
	ds_read_b128 v[172:175], v226 offset:4096
	ds_read_b128 v[176:179], v226 offset:5120
	ds_read_b128 v[164:167], v226 offset:6144
	ds_read_b128 v[168:171], v226 offset:7168
	global_load_lds_dwordx4 v[216:217], off
	v_lshl_add_u64 v[216:217], v[214:215], 0, s[58:59]
	s_add_i32 m0, s74, 0xe000
	s_and_b64 vcc, exec, s[68:69]
	global_load_lds_dwordx4 v[216:217], off
	s_cbranch_vccz .Lpeelg0_802
	s_waitcnt vmcnt(8)
	s_mov_b64 s[26:27], 0

.Lpeelg0_804:
	s_add_u32 s9, s40, s58
	s_addc_u32 s10, s41, s59
	s_add_u32 s9, s9, 0x100
	s_addc_u32 s10, s10, 0
	s_add_u32 s11, s70, s58
	s_addc_u32 s12, s71, s59
	s_waitcnt lgkmcnt(0)
	s_cmpk_eq_i32 s58, 0x700
	s_cselect_b32 s67, s53, s10
	s_cselect_b32 s66, s52, s9
	s_cselect_b32 s37, s55, s12
	s_cselect_b32 s36, s54, s11
	s_barrier
	s_setprio 1
	s_waitcnt lgkmcnt(0)
	v_mfma_f32_16x16x32_bf16 v[128:131], v[148:151], v[188:191], 0
	v_mfma_f32_16x16x32_bf16 v[124:127], v[156:159], v[188:191], 0
	v_mfma_f32_16x16x32_bf16 v[112:115], v[148:151], v[180:183], 0
	v_mfma_f32_16x16x32_bf16 v[108:111], v[156:159], v[180:183], 0
	v_mfma_f32_16x16x32_bf16 v[96:99], v[148:151], v[172:175], 0
	v_mfma_f32_16x16x32_bf16 v[92:95], v[156:159], v[172:175], 0
	v_mfma_f32_16x16x32_bf16 v[80:83], v[148:151], v[164:167], 0
	v_mfma_f32_16x16x32_bf16 v[76:79], v[156:159], v[164:167], 0
	v_mfma_f32_16x16x32_bf16 v[128:131], v[152:155], v[192:195], v[128:131]
	v_mfma_f32_16x16x32_bf16 v[124:127], v[160:163], v[192:195], v[124:127]
	v_mfma_f32_16x16x32_bf16 v[112:115], v[152:155], v[184:187], v[112:115]
	v_mfma_f32_16x16x32_bf16 v[108:111], v[160:163], v[184:187], v[108:111]
	v_mfma_f32_16x16x32_bf16 v[96:99], v[152:155], v[176:179], v[96:99]
	v_mfma_f32_16x16x32_bf16 v[92:95], v[160:163], v[176:179], v[92:95]
	v_mfma_f32_16x16x32_bf16 v[80:83], v[152:155], v[168:171], v[80:83]
	v_mfma_f32_16x16x32_bf16 v[76:79], v[160:163], v[168:171], v[76:79]
	s_setprio 0
	s_setprio 1
	v_mfma_f32_16x16x32_bf16 v[120:123], v[132:135], v[188:191], 0
	v_mfma_f32_16x16x32_bf16 v[116:119], v[140:143], v[188:191], 0
	v_mfma_f32_16x16x32_bf16 v[104:107], v[132:135], v[180:183], 0
	v_mfma_f32_16x16x32_bf16 v[100:103], v[140:143], v[180:183], 0
	v_mfma_f32_16x16x32_bf16 v[88:91], v[132:135], v[172:175], 0
	v_mfma_f32_16x16x32_bf16 v[84:87], v[140:143], v[172:175], 0
	v_mfma_f32_16x16x32_bf16 v[72:75], v[132:135], v[164:167], 0
	v_mfma_f32_16x16x32_bf16 v[68:71], v[140:143], v[164:167], 0
	v_mfma_f32_16x16x32_bf16 v[120:123], v[136:139], v[192:195], v[120:123]
	v_mfma_f32_16x16x32_bf16 v[116:119], v[144:147], v[192:195], v[116:119]
	v_mfma_f32_16x16x32_bf16 v[104:107], v[136:139], v[184:187], v[104:107]
	v_mfma_f32_16x16x32_bf16 v[100:103], v[144:147], v[184:187], v[100:103]
	v_mfma_f32_16x16x32_bf16 v[88:91], v[136:139], v[176:179], v[88:91]
	v_mfma_f32_16x16x32_bf16 v[84:87], v[144:147], v[176:179], v[84:87]
	v_mfma_f32_16x16x32_bf16 v[72:75], v[136:139], v[168:171], v[72:75]
	v_mfma_f32_16x16x32_bf16 v[68:71], v[144:147], v[168:171], v[68:71]
	s_setprio 0
	s_barrier
	s_mov_b32 m0, s75
	v_lshl_add_u64 v[222:223], s[36:37], 0, v[198:199]
	s_add_u32 s10, s36, 0x40000
	ds_read_b128 v[188:191], v226 offset:16384
	ds_read_b128 v[192:195], v226 offset:17408
	ds_read_b128 v[180:183], v226 offset:18432
	ds_read_b128 v[184:187], v226 offset:19456
	ds_read_b128 v[172:175], v226 offset:20480
	ds_read_b128 v[176:179], v226 offset:21504
	ds_read_b128 v[164:167], v226 offset:22528
	ds_read_b128 v[168:171], v226 offset:23552
	global_load_lds_dwordx4 v[222:223], off
	v_lshl_add_u64 v[220:221], s[36:37], 0, v[202:203]
	s_mov_b32 m0, s84
	s_addc_u32 s11, s37, 0
	global_load_lds_dwordx4 v[220:221], off
	v_lshl_add_u64 v[216:217], s[10:11], 0, v[198:199]
	s_mov_b32 m0, s85
	v_lshl_add_u64 v[218:219], s[66:67], 0, v[200:201]
	global_load_lds_dwordx4 v[216:217], off
	v_lshl_add_u64 v[216:217], s[10:11], 0, v[202:203]
	s_mov_b32 m0, s86
	s_mov_b64 s[26:27], -1
	global_load_lds_dwordx4 v[216:217], off
	v_lshl_add_u64 v[216:217], s[66:67], 0, v[196:197]
	s_mov_b32 m0, s74
	s_and_b64 vcc, exec, s[68:69]
	global_load_lds_dwordx4 v[216:217], off
	s_mov_b32 m0, s87
	s_nop 0
	global_load_lds_dwordx4 v[218:219], off
	s_cbranch_vccz .Lpeelg0_806
	s_waitcnt vmcnt(8)
	s_mov_b64 s[26:27], 0

.Lpeelg0_T:
	s_waitcnt lgkmcnt(0)
	s_barrier
	s_setprio 1
	s_waitcnt lgkmcnt(0)
	v_mfma_f32_16x16x32_bf16 v[62:65], v[148:151], v[188:191], 0
	v_mfma_f32_16x16x32_bf16 v[58:61], v[156:159], v[188:191], 0
	v_mfma_f32_16x16x32_bf16 v[46:49], v[148:151], v[180:183], 0
	v_mfma_f32_16x16x32_bf16 v[42:45], v[156:159], v[180:183], 0
	v_mfma_f32_16x16x32_bf16 v[30:33], v[148:151], v[172:175], 0
	v_mfma_f32_16x16x32_bf16 v[26:29], v[156:159], v[172:175], 0
	v_mfma_f32_16x16x32_bf16 v[14:17], v[148:151], v[164:167], 0
	v_mfma_f32_16x16x32_bf16 v[10:13], v[156:159], v[164:167], 0
	v_mfma_f32_16x16x32_bf16 v[62:65], v[152:155], v[192:195], v[62:65]
	v_mfma_f32_16x16x32_bf16 v[58:61], v[160:163], v[192:195], v[58:61]
	v_mfma_f32_16x16x32_bf16 v[46:49], v[152:155], v[184:187], v[46:49]
	v_mfma_f32_16x16x32_bf16 v[42:45], v[160:163], v[184:187], v[42:45]
	v_mfma_f32_16x16x32_bf16 v[30:33], v[152:155], v[176:179], v[30:33]
	v_mfma_f32_16x16x32_bf16 v[26:29], v[160:163], v[176:179], v[26:29]
	v_mfma_f32_16x16x32_bf16 v[14:17], v[152:155], v[168:171], v[14:17]
	v_mfma_f32_16x16x32_bf16 v[10:13], v[160:163], v[168:171], v[10:13]
	s_setprio 0
	s_setprio 1
	v_mfma_f32_16x16x32_bf16 v[54:57], v[132:135], v[188:191], 0
	v_mfma_f32_16x16x32_bf16 v[50:53], v[140:143], v[188:191], 0
	v_mfma_f32_16x16x32_bf16 v[38:41], v[132:135], v[180:183], 0
	v_mfma_f32_16x16x32_bf16 v[34:37], v[140:143], v[180:183], 0
	v_mfma_f32_16x16x32_bf16 v[22:25], v[132:135], v[172:175], 0
	v_mfma_f32_16x16x32_bf16 v[18:21], v[140:143], v[172:175], 0
	v_mfma_f32_16x16x32_bf16 v[6:9], v[132:135], v[164:167], 0
	v_mfma_f32_16x16x32_bf16 v[2:5], v[140:143], v[164:167], 0
	v_mfma_f32_16x16x32_bf16 v[54:57], v[136:139], v[192:195], v[54:57]
	v_mfma_f32_16x16x32_bf16 v[50:53], v[144:147], v[192:195], v[50:53]
	v_mfma_f32_16x16x32_bf16 v[38:41], v[136:139], v[184:187], v[38:41]
	v_mfma_f32_16x16x32_bf16 v[34:37], v[144:147], v[184:187], v[34:37]
	v_mfma_f32_16x16x32_bf16 v[22:25], v[136:139], v[176:179], v[22:25]
	v_mfma_f32_16x16x32_bf16 v[18:21], v[144:147], v[176:179], v[18:21]
	v_mfma_f32_16x16x32_bf16 v[6:9], v[136:139], v[168:171], v[6:9]
	v_mfma_f32_16x16x32_bf16 v[2:5], v[144:147], v[168:171], v[2:5]
	s_setprio 0
	s_barrier
	s_add_i32 s9, 0, 0x18000
	s_add_i32 s12, 0, 0x1c000
	v_add_u32_e32 v144, s9, v225
	v_add_u32_e32 v160, s12, v225
	ds_read_b128 v[132:135], v144
	ds_read_b128 v[136:139], v144 offset:1024
	ds_read_b128 v[140:143], v144 offset:2048
	ds_read_b128 v[144:147], v144 offset:3072
	ds_read_b128 v[148:151], v160
	ds_read_b128 v[152:155], v160 offset:1024
	ds_read_b128 v[156:159], v160 offset:2048
	ds_read_b128 v[160:163], v160 offset:3072
	s_add_u32 s10, s66, 0x100000
	s_addc_u32 s11, s67, 0
	s_mov_b32 m0, s88
	v_lshl_add_u64 v[228:229], s[10:11], 0, v[196:197]
	ds_read_b128 v[164:167], v226 offset:32768
	ds_read_b128 v[168:171], v226 offset:33792
	ds_read_b128 v[172:175], v226 offset:34816
	ds_read_b128 v[176:179], v226 offset:35840
	ds_read_b128 v[180:183], v226 offset:36864
	ds_read_b128 v[184:187], v226 offset:37888
	ds_read_b128 v[188:191], v226 offset:38912
	ds_read_b128 v[192:195], v226 offset:39936
	global_load_lds_dwordx4 v[228:229], off
	v_lshl_add_u64 v[228:229], s[10:11], 0, v[200:201]
	s_mov_b32 m0, s89
	s_nop 0
	global_load_lds_dwordx4 v[228:229], off
	s_waitcnt vmcnt(8)
	s_waitcnt lgkmcnt(0)
	s_barrier
	s_setprio 1
	s_waitcnt lgkmcnt(0)
	v_mfma_f32_16x16x32_bf16 v[128:131], v[132:135], v[164:167], v[128:131]
	v_mfma_f32_16x16x32_bf16 v[124:127], v[140:143], v[164:167], v[124:127]
	v_mfma_f32_16x16x32_bf16 v[112:115], v[132:135], v[172:175], v[112:115]
	v_mfma_f32_16x16x32_bf16 v[108:111], v[140:143], v[172:175], v[108:111]
	v_mfma_f32_16x16x32_bf16 v[96:99], v[132:135], v[180:183], v[96:99]
	v_mfma_f32_16x16x32_bf16 v[92:95], v[140:143], v[180:183], v[92:95]
	v_mfma_f32_16x16x32_bf16 v[80:83], v[132:135], v[188:191], v[80:83]
	v_mfma_f32_16x16x32_bf16 v[76:79], v[140:143], v[188:191], v[76:79]
	v_mfma_f32_16x16x32_bf16 v[128:131], v[136:139], v[168:171], v[128:131]
	v_mfma_f32_16x16x32_bf16 v[124:127], v[144:147], v[168:171], v[124:127]
	v_mfma_f32_16x16x32_bf16 v[112:115], v[136:139], v[176:179], v[112:115]
	v_mfma_f32_16x16x32_bf16 v[108:111], v[144:147], v[176:179], v[108:111]
	v_mfma_f32_16x16x32_bf16 v[96:99], v[136:139], v[184:187], v[96:99]
	v_mfma_f32_16x16x32_bf16 v[92:95], v[144:147], v[184:187], v[92:95]
	v_mfma_f32_16x16x32_bf16 v[80:83], v[136:139], v[192:195], v[80:83]
	v_mfma_f32_16x16x32_bf16 v[76:79], v[144:147], v[192:195], v[76:79]
	s_setprio 0
	s_setprio 1
	v_mfma_f32_16x16x32_bf16 v[120:123], v[148:151], v[164:167], v[120:123]
	v_mfma_f32_16x16x32_bf16 v[116:119], v[156:159], v[164:167], v[116:119]
	v_mfma_f32_16x16x32_bf16 v[104:107], v[148:151], v[172:175], v[104:107]
	v_mfma_f32_16x16x32_bf16 v[100:103], v[156:159], v[172:175], v[100:103]
	v_mfma_f32_16x16x32_bf16 v[88:91], v[148:151], v[180:183], v[88:91]
	v_mfma_f32_16x16x32_bf16 v[84:87], v[156:159], v[180:183], v[84:87]
	v_mfma_f32_16x16x32_bf16 v[72:75], v[148:151], v[188:191], v[72:75]
	v_mfma_f32_16x16x32_bf16 v[68:71], v[156:159], v[188:191], v[68:71]
	v_mfma_f32_16x16x32_bf16 v[120:123], v[152:155], v[168:171], v[120:123]
	v_mfma_f32_16x16x32_bf16 v[116:119], v[160:163], v[168:171], v[116:119]
	v_mfma_f32_16x16x32_bf16 v[104:107], v[152:155], v[176:179], v[104:107]
	v_mfma_f32_16x16x32_bf16 v[100:103], v[160:163], v[176:179], v[100:103]
	v_mfma_f32_16x16x32_bf16 v[88:91], v[152:155], v[184:187], v[88:91]
	v_mfma_f32_16x16x32_bf16 v[84:87], v[160:163], v[184:187], v[84:87]
	v_mfma_f32_16x16x32_bf16 v[72:75], v[152:155], v[192:195], v[72:75]
	v_mfma_f32_16x16x32_bf16 v[68:71], v[160:163], v[192:195], v[68:71]
	s_setprio 0
	s_barrier
	s_add_i32 s9, s9, s72
	v_lshl_add_u64 v[222:223], v[222:223], 0, s[60:61]
	s_mov_b32 m0, s9
	ds_read_b128 v[164:167], v226 offset:49152
	ds_read_b128 v[168:171], v226 offset:50176
	ds_read_b128 v[172:175], v226 offset:51200
	ds_read_b128 v[176:179], v226 offset:52224
	ds_read_b128 v[180:183], v226 offset:53248
	ds_read_b128 v[184:187], v226 offset:54272
	ds_read_b128 v[188:191], v226 offset:55296
	ds_read_b128 v[192:195], v226 offset:56320
	global_load_lds_dwordx4 v[222:223], off
	s_add_i32 m0, s9, 0x2000
	s_add_u32 s10, s36, 0x40080
	v_lshl_add_u64 v[220:221], v[220:221], 0, s[60:61]
	s_addc_u32 s11, s37, 0
	s_add_i32 s9, s12, s72
	global_load_lds_dwordx4 v[220:221], off
	v_lshl_add_u64 v[220:221], s[10:11], 0, v[198:199]
	s_mov_b32 m0, s9
	v_lshl_add_u64 v[216:217], v[216:217], 0, s[60:61]
	global_load_lds_dwordx4 v[220:221], off
	v_lshl_add_u64 v[220:221], s[10:11], 0, v[202:203]
	s_add_i32 m0, s9, 0x2000
	s_nop 0
	global_load_lds_dwordx4 v[220:221], off
	s_mov_b32 m0, s91
	s_nop 0
	global_load_lds_dwordx4 v[216:217], off
	v_lshl_add_u64 v[216:217], v[218:219], 0, s[60:61]
	s_mov_b32 m0, s92
	s_nop 0
	global_load_lds_dwordx4 v[216:217], off
	s_waitcnt vmcnt(8)
	s_waitcnt lgkmcnt(0)
	s_barrier
	s_setprio 1
	s_waitcnt lgkmcnt(0)
	v_mfma_f32_16x16x32_bf16 v[62:65], v[132:135], v[164:167], v[62:65]
	v_mfma_f32_16x16x32_bf16 v[58:61], v[140:143], v[164:167], v[58:61]
	v_mfma_f32_16x16x32_bf16 v[46:49], v[132:135], v[172:175], v[46:49]
	v_mfma_f32_16x16x32_bf16 v[42:45], v[140:143], v[172:175], v[42:45]
	v_mfma_f32_16x16x32_bf16 v[30:33], v[132:135], v[180:183], v[30:33]
	v_mfma_f32_16x16x32_bf16 v[26:29], v[140:143], v[180:183], v[26:29]
	v_mfma_f32_16x16x32_bf16 v[14:17], v[132:135], v[188:191], v[14:17]
	v_mfma_f32_16x16x32_bf16 v[10:13], v[140:143], v[188:191], v[10:13]
	v_mfma_f32_16x16x32_bf16 v[62:65], v[136:139], v[168:171], v[62:65]
	v_mfma_f32_16x16x32_bf16 v[58:61], v[144:147], v[168:171], v[58:61]
	v_mfma_f32_16x16x32_bf16 v[46:49], v[136:139], v[176:179], v[46:49]
	v_mfma_f32_16x16x32_bf16 v[42:45], v[144:147], v[176:179], v[42:45]
	v_mfma_f32_16x16x32_bf16 v[30:33], v[136:139], v[184:187], v[30:33]
	v_mfma_f32_16x16x32_bf16 v[26:29], v[144:147], v[184:187], v[26:29]
	v_mfma_f32_16x16x32_bf16 v[14:17], v[136:139], v[192:195], v[14:17]
	v_mfma_f32_16x16x32_bf16 v[10:13], v[144:147], v[192:195], v[10:13]
	s_setprio 0
	s_setprio 1
	v_mfma_f32_16x16x32_bf16 v[54:57], v[148:151], v[164:167], v[54:57]
	v_mfma_f32_16x16x32_bf16 v[50:53], v[156:159], v[164:167], v[50:53]
	v_mfma_f32_16x16x32_bf16 v[38:41], v[148:151], v[172:175], v[38:41]
	v_mfma_f32_16x16x32_bf16 v[34:37], v[156:159], v[172:175], v[34:37]
	v_mfma_f32_16x16x32_bf16 v[22:25], v[148:151], v[180:183], v[22:25]
	v_mfma_f32_16x16x32_bf16 v[18:21], v[156:159], v[180:183], v[18:21]
	v_mfma_f32_16x16x32_bf16 v[6:9], v[148:151], v[188:191], v[6:9]
	v_mfma_f32_16x16x32_bf16 v[2:5], v[156:159], v[188:191], v[2:5]
	v_mfma_f32_16x16x32_bf16 v[54:57], v[152:155], v[168:171], v[54:57]
	v_mfma_f32_16x16x32_bf16 v[50:53], v[160:163], v[168:171], v[50:53]
	v_mfma_f32_16x16x32_bf16 v[38:41], v[152:155], v[176:179], v[38:41]
	v_mfma_f32_16x16x32_bf16 v[34:37], v[160:163], v[176:179], v[34:37]
	v_mfma_f32_16x16x32_bf16 v[22:25], v[152:155], v[184:187], v[22:25]
	v_mfma_f32_16x16x32_bf16 v[18:21], v[160:163], v[184:187], v[18:21]
	v_mfma_f32_16x16x32_bf16 v[6:9], v[152:155], v[192:195], v[6:9]
	v_mfma_f32_16x16x32_bf16 v[2:5], v[160:163], v[192:195], v[2:5]
	s_setprio 0
	s_barrier
	s_add_i32 s8, s8, 2
	s_add_u32 s58, s58, 0x100
	s_addc_u32 s59, s59, 0
	s_cmp_gt_u32 s8, 13
	s_cbranch_scc1 .LBB0_808
	s_branch .LBB0_800

.LBB0_1237:
	v_mov_b32_e32 v209, v67
	v_mov_b32_e32 v213, v67
	s_mov_b64 s[8:9], 0x100
	v_mov_b32_e32 v50, 0
	v_lshl_add_u64 v[216:217], s[48:49], 0, v[212:213]
	v_lshl_add_u64 v[218:219], s[48:49], 0, v[208:209]
	v_lshl_add_u64 v[220:221], v[2:3], 0, s[8:9]
	s_mov_b32 s45, -2
	s_mov_b64 s[36:37], 0
	s_xor_b64 s[34:35], s[34:35], -1
	v_add_u32_e32 v66, 0, v236
	v_add_u32_e32 v132, 0x10000, v66
	v_add_u32_e32 v66, 0x14000, v66
	ds_read_b128 v[148:151], v132
	ds_read_b128 v[152:155], v132 offset:1024
	ds_read_b128 v[156:159], v132 offset:2048
	ds_read_b128 v[160:163], v132 offset:3072
	ds_read_b128 v[132:135], v66
	ds_read_b128 v[136:139], v66 offset:1024
	ds_read_b128 v[140:143], v66 offset:2048
	ds_read_b128 v[144:147], v66 offset:3072
	s_cmp_lg_u32 s36, 0
	s_cselect_b64 s[8:9], -1, 0
	s_mov_b64 s[26:27], -1
	s_or_b64 s[86:87], s[34:35], s[8:9]
	v_lshl_add_u64 v[222:223], v[218:219], 0, s[36:37]
	s_add_i32 m0, s90, 0xc000
	ds_read_b128 v[188:191], v211
	ds_read_b128 v[192:195], v211 offset:1024
	ds_read_b128 v[180:183], v211 offset:2048
	ds_read_b128 v[184:187], v211 offset:3072
	ds_read_b128 v[172:175], v211 offset:4096
	ds_read_b128 v[176:179], v211 offset:5120
	ds_read_b128 v[164:167], v211 offset:6144
	ds_read_b128 v[168:171], v211 offset:7168
	global_load_lds_dwordx4 v[222:223], off
	v_lshl_add_u64 v[222:223], v[216:217], 0, s[36:37]
	s_add_i32 m0, s90, 0xe000
	s_and_b64 vcc, exec, s[86:87]
	global_load_lds_dwordx4 v[222:223], off
	s_cbranch_vccz .Lpeelg1_1241
	s_waitcnt vmcnt(8)
	s_mov_b64 s[26:27], 0

.Lpeelg1_1243:
	s_add_u32 s84, s36, 0x100
	s_addc_u32 s85, s37, 0
	s_cmpk_eq_i32 s36, 0x700
	s_cselect_b64 s[42:43], -1, 0
	s_and_b64 s[8:9], s[42:43], exec
	s_cselect_b32 s9, 0, s84
	s_waitcnt lgkmcnt(0)
	v_lshl_add_u64 v[222:223], v[220:221], 0, s[36:37]
	s_cselect_b32 s8, 0, s85
	s_add_u32 s36, s66, s9
	v_cndmask_b32_e64 v223, v223, v203, s[42:43]
	s_addc_u32 s37, s67, s8
	v_cndmask_b32_e64 v222, v222, v202, s[42:43]
	s_barrier
	s_setprio 1
	s_waitcnt lgkmcnt(0)
	v_mfma_f32_16x16x32_bf16 v[128:131], v[148:151], v[188:191], 0
	v_mfma_f32_16x16x32_bf16 v[120:123], v[156:159], v[188:191], 0
	v_mfma_f32_16x16x32_bf16 v[112:115], v[148:151], v[180:183], 0
	v_mfma_f32_16x16x32_bf16 v[104:107], v[156:159], v[180:183], 0
	v_mfma_f32_16x16x32_bf16 v[96:99], v[148:151], v[172:175], 0
	v_mfma_f32_16x16x32_bf16 v[88:91], v[156:159], v[172:175], 0
	v_mfma_f32_16x16x32_bf16 v[80:83], v[148:151], v[164:167], 0
	v_mfma_f32_16x16x32_bf16 v[72:75], v[156:159], v[164:167], 0
	v_mfma_f32_16x16x32_bf16 v[128:131], v[152:155], v[192:195], v[128:131]
	v_mfma_f32_16x16x32_bf16 v[120:123], v[160:163], v[192:195], v[120:123]
	v_mfma_f32_16x16x32_bf16 v[112:115], v[152:155], v[184:187], v[112:115]
	v_mfma_f32_16x16x32_bf16 v[104:107], v[160:163], v[184:187], v[104:107]
	v_mfma_f32_16x16x32_bf16 v[96:99], v[152:155], v[176:179], v[96:99]
	v_mfma_f32_16x16x32_bf16 v[88:91], v[160:163], v[176:179], v[88:91]
	v_mfma_f32_16x16x32_bf16 v[80:83], v[152:155], v[168:171], v[80:83]
	v_mfma_f32_16x16x32_bf16 v[72:75], v[160:163], v[168:171], v[72:75]
	s_setprio 0
	s_setprio 1
	v_mfma_f32_16x16x32_bf16 v[124:127], v[132:135], v[188:191], 0
	v_mfma_f32_16x16x32_bf16 v[116:119], v[140:143], v[188:191], 0
	v_mfma_f32_16x16x32_bf16 v[108:111], v[132:135], v[180:183], 0
	v_mfma_f32_16x16x32_bf16 v[100:103], v[140:143], v[180:183], 0
	v_mfma_f32_16x16x32_bf16 v[92:95], v[132:135], v[172:175], 0
	v_mfma_f32_16x16x32_bf16 v[84:87], v[140:143], v[172:175], 0
	v_mfma_f32_16x16x32_bf16 v[76:79], v[132:135], v[164:167], 0
	v_mfma_f32_16x16x32_bf16 v[68:71], v[140:143], v[164:167], 0
	v_mfma_f32_16x16x32_bf16 v[124:127], v[136:139], v[192:195], v[124:127]
	v_mfma_f32_16x16x32_bf16 v[116:119], v[144:147], v[192:195], v[116:119]
	v_mfma_f32_16x16x32_bf16 v[108:111], v[136:139], v[184:187], v[108:111]
	v_mfma_f32_16x16x32_bf16 v[100:103], v[144:147], v[184:187], v[100:103]
	v_mfma_f32_16x16x32_bf16 v[92:95], v[136:139], v[176:179], v[92:95]
	v_mfma_f32_16x16x32_bf16 v[84:87], v[144:147], v[176:179], v[84:87]
	v_mfma_f32_16x16x32_bf16 v[76:79], v[136:139], v[168:171], v[76:79]
	v_mfma_f32_16x16x32_bf16 v[68:71], v[144:147], v[168:171], v[68:71]
	s_setprio 0
	s_barrier
	s_mov_b32 m0, s91
	v_lshl_add_u64 v[226:227], v[222:223], 0, v[196:197]
	ds_read_b128 v[188:191], v211 offset:16384
	ds_read_b128 v[192:195], v211 offset:17408
	ds_read_b128 v[180:183], v211 offset:18432
	ds_read_b128 v[184:187], v211 offset:19456
	ds_read_b128 v[172:175], v211 offset:20480
	ds_read_b128 v[176:179], v211 offset:21504
	ds_read_b128 v[164:167], v211 offset:22528
	ds_read_b128 v[168:171], v211 offset:23552
	global_load_lds_dwordx4 v[226:227], off
	v_lshl_add_u64 v[224:225], v[222:223], 0, v[198:199]
	s_mov_b32 m0, s92
	v_lshl_add_u64 v[228:229], v[222:223], 0, s[78:79]
	global_load_lds_dwordx4 v[224:225], off
	v_lshl_add_u64 v[244:245], v[228:229], 0, v[196:197]
	s_mov_b32 m0, s93
	v_lshl_add_u64 v[228:229], v[228:229], 0, v[198:199]
	global_load_lds_dwordx4 v[244:245], off
	s_mov_b32 m0, s94
	v_cndmask_b32_e64 v66, v210, v238, s[42:43]
	global_load_lds_dwordx4 v[228:229], off
	s_mov_b32 m0, s90
	v_cndmask_b32_e64 v228, v214, v240, s[42:43]
	global_load_lds_dwordx4 v66, s[36:37]
	s_mov_b32 m0, s95
	s_mov_b64 s[26:27], -1
	global_load_lds_dwordx4 v228, s[36:37]
	s_and_b64 vcc, exec, s[86:87]
	s_cbranch_vccz .Lpeelg1_1245
	s_waitcnt vmcnt(8)
	s_mov_b64 s[26:27], 0

.Lpeelg1_T:
	s_waitcnt lgkmcnt(0)
	v_mov_b32_e32 v229, v67
	v_lshl_add_u64 v[244:245], s[36:37], 0, v[66:67]
	v_lshl_add_u64 v[228:229], s[36:37], 0, v[228:229]
	s_barrier
	s_setprio 1
	s_waitcnt lgkmcnt(0)
	v_mfma_f32_16x16x32_bf16 v[62:65], v[148:151], v[188:191], 0
	v_mfma_f32_16x16x32_bf16 v[54:57], v[156:159], v[188:191], 0
	v_mfma_f32_16x16x32_bf16 v[38:41], v[148:151], v[180:183], 0
	v_mfma_f32_16x16x32_bf16 v[34:37], v[156:159], v[180:183], 0
	v_mfma_f32_16x16x32_bf16 v[22:25], v[148:151], v[172:175], 0
	v_mfma_f32_16x16x32_bf16 v[18:21], v[156:159], v[172:175], 0
	v_mfma_f32_16x16x32_bf16 v[6:9], v[148:151], v[164:167], 0
	v_mfma_f32_16x16x32_bf16 v[2:5], v[156:159], v[164:167], 0
	v_mfma_f32_16x16x32_bf16 v[62:65], v[152:155], v[192:195], v[62:65]
	v_mfma_f32_16x16x32_bf16 v[54:57], v[160:163], v[192:195], v[54:57]
	v_mfma_f32_16x16x32_bf16 v[38:41], v[152:155], v[184:187], v[38:41]
	v_mfma_f32_16x16x32_bf16 v[34:37], v[160:163], v[184:187], v[34:37]
	v_mfma_f32_16x16x32_bf16 v[22:25], v[152:155], v[176:179], v[22:25]
	v_mfma_f32_16x16x32_bf16 v[18:21], v[160:163], v[176:179], v[18:21]
	v_mfma_f32_16x16x32_bf16 v[6:9], v[152:155], v[168:171], v[6:9]
	v_mfma_f32_16x16x32_bf16 v[2:5], v[160:163], v[168:171], v[2:5]
	s_setprio 0
	s_setprio 1
	v_mfma_f32_16x16x32_bf16 v[58:61], v[132:135], v[188:191], 0
	v_mfma_f32_16x16x32_bf16 v[50:53], v[140:143], v[188:191], 0
	v_mfma_f32_16x16x32_bf16 v[46:49], v[132:135], v[180:183], 0
	v_mfma_f32_16x16x32_bf16 v[42:45], v[140:143], v[180:183], 0
	v_mfma_f32_16x16x32_bf16 v[30:33], v[132:135], v[172:175], 0
	v_mfma_f32_16x16x32_bf16 v[26:29], v[140:143], v[172:175], 0
	v_mfma_f32_16x16x32_bf16 v[14:17], v[132:135], v[164:167], 0
	v_mfma_f32_16x16x32_bf16 v[10:13], v[140:143], v[164:167], 0
	v_mfma_f32_16x16x32_bf16 v[58:61], v[136:139], v[192:195], v[58:61]
	v_mfma_f32_16x16x32_bf16 v[50:53], v[144:147], v[192:195], v[50:53]
	v_mfma_f32_16x16x32_bf16 v[46:49], v[136:139], v[184:187], v[46:49]
	v_mfma_f32_16x16x32_bf16 v[42:45], v[144:147], v[184:187], v[42:45]
	v_mfma_f32_16x16x32_bf16 v[30:33], v[136:139], v[176:179], v[30:33]
	v_mfma_f32_16x16x32_bf16 v[26:29], v[144:147], v[176:179], v[26:29]
	v_mfma_f32_16x16x32_bf16 v[14:17], v[136:139], v[168:171], v[14:17]
	v_mfma_f32_16x16x32_bf16 v[10:13], v[144:147], v[168:171], v[10:13]
	s_setprio 0
	s_barrier
	s_add_i32 s8, 0, 0x18000
	v_add_u32_e32 v66, s8, v236
	s_add_i32 s9, 0, 0x1c000
	ds_read_b128 v[132:135], v66
	ds_read_b128 v[136:139], v66 offset:1024
	ds_read_b128 v[140:143], v66 offset:2048
	ds_read_b128 v[144:147], v66 offset:3072
	v_add_u32_e32 v66, s9, v236
	ds_read_b128 v[148:151], v66
	ds_read_b128 v[152:155], v66 offset:1024
	ds_read_b128 v[156:159], v66 offset:2048
	ds_read_b128 v[160:163], v66 offset:3072
	s_mov_b32 m0, s96
	v_cndmask_b32_e64 v66, v208, v239, s[42:43]
	ds_read_b128 v[164:167], v211 offset:32768
	ds_read_b128 v[168:171], v211 offset:33792
	ds_read_b128 v[172:175], v211 offset:34816
	ds_read_b128 v[176:179], v211 offset:35840
	ds_read_b128 v[180:183], v211 offset:36864
	ds_read_b128 v[184:187], v211 offset:37888
	ds_read_b128 v[188:191], v211 offset:38912
	ds_read_b128 v[192:195], v211 offset:39936
	v_cndmask_b32_e64 v209, v212, v241, s[42:43]
	global_load_lds_dwordx4 v66, s[36:37]
	s_mov_b32 m0, s97
	s_nop 0
	global_load_lds_dwordx4 v209, s[36:37]
	s_waitcnt vmcnt(8)
	s_waitcnt lgkmcnt(0)
	s_barrier
	s_setprio 1
	s_waitcnt lgkmcnt(0)
	v_mfma_f32_16x16x32_bf16 v[128:131], v[132:135], v[164:167], v[128:131]
	v_mfma_f32_16x16x32_bf16 v[120:123], v[140:143], v[164:167], v[120:123]
	v_mfma_f32_16x16x32_bf16 v[112:115], v[132:135], v[172:175], v[112:115]
	v_mfma_f32_16x16x32_bf16 v[104:107], v[140:143], v[172:175], v[104:107]
	v_mfma_f32_16x16x32_bf16 v[96:99], v[132:135], v[180:183], v[96:99]
	v_mfma_f32_16x16x32_bf16 v[88:91], v[140:143], v[180:183], v[88:91]
	v_mfma_f32_16x16x32_bf16 v[80:83], v[132:135], v[188:191], v[80:83]
	v_mfma_f32_16x16x32_bf16 v[72:75], v[140:143], v[188:191], v[72:75]
	v_mfma_f32_16x16x32_bf16 v[128:131], v[136:139], v[168:171], v[128:131]
	v_mfma_f32_16x16x32_bf16 v[120:123], v[144:147], v[168:171], v[120:123]
	v_mfma_f32_16x16x32_bf16 v[112:115], v[136:139], v[176:179], v[112:115]
	v_mfma_f32_16x16x32_bf16 v[104:107], v[144:147], v[176:179], v[104:107]
	v_mfma_f32_16x16x32_bf16 v[96:99], v[136:139], v[184:187], v[96:99]
	v_mfma_f32_16x16x32_bf16 v[88:91], v[144:147], v[184:187], v[88:91]
	v_mfma_f32_16x16x32_bf16 v[80:83], v[136:139], v[192:195], v[80:83]
	v_mfma_f32_16x16x32_bf16 v[72:75], v[144:147], v[192:195], v[72:75]
	s_setprio 0
	s_setprio 1
	v_mfma_f32_16x16x32_bf16 v[124:127], v[148:151], v[164:167], v[124:127]
	v_mfma_f32_16x16x32_bf16 v[116:119], v[156:159], v[164:167], v[116:119]
	v_mfma_f32_16x16x32_bf16 v[108:111], v[148:151], v[172:175], v[108:111]
	v_mfma_f32_16x16x32_bf16 v[100:103], v[156:159], v[172:175], v[100:103]
	v_mfma_f32_16x16x32_bf16 v[92:95], v[148:151], v[180:183], v[92:95]
	v_mfma_f32_16x16x32_bf16 v[84:87], v[156:159], v[180:183], v[84:87]
	v_mfma_f32_16x16x32_bf16 v[76:79], v[148:151], v[188:191], v[76:79]
	v_mfma_f32_16x16x32_bf16 v[68:71], v[156:159], v[188:191], v[68:71]
	v_mfma_f32_16x16x32_bf16 v[124:127], v[152:155], v[168:171], v[124:127]
	v_mfma_f32_16x16x32_bf16 v[116:119], v[160:163], v[168:171], v[116:119]
	v_mfma_f32_16x16x32_bf16 v[108:111], v[152:155], v[176:179], v[108:111]
	v_mfma_f32_16x16x32_bf16 v[100:103], v[160:163], v[176:179], v[100:103]
	v_mfma_f32_16x16x32_bf16 v[92:95], v[152:155], v[184:187], v[92:95]
	v_mfma_f32_16x16x32_bf16 v[84:87], v[160:163], v[184:187], v[84:87]
	v_mfma_f32_16x16x32_bf16 v[76:79], v[152:155], v[192:195], v[76:79]
	v_mfma_f32_16x16x32_bf16 v[68:71], v[160:163], v[192:195], v[68:71]
	s_setprio 0
	s_barrier
	s_add_i32 s8, s8, s89
	v_lshl_add_u64 v[226:227], v[226:227], 0, s[60:61]
	s_mov_b32 m0, s8
	ds_read_b128 v[164:167], v211 offset:49152
	ds_read_b128 v[168:171], v211 offset:50176
	ds_read_b128 v[172:175], v211 offset:51200
	ds_read_b128 v[176:179], v211 offset:52224
	ds_read_b128 v[180:183], v211 offset:53248
	ds_read_b128 v[184:187], v211 offset:54272
	ds_read_b128 v[188:191], v211 offset:55296
	ds_read_b128 v[192:195], v211 offset:56320
	global_load_lds_dwordx4 v[226:227], off
	v_lshl_add_u64 v[224:225], v[224:225], 0, s[60:61]
	s_add_i32 m0, s8, 0x2000
	v_lshl_add_u64 v[222:223], v[222:223], 0, s[30:31]
	s_add_i32 s8, s9, s89
	global_load_lds_dwordx4 v[224:225], off
	v_lshl_add_u64 v[224:225], v[222:223], 0, v[196:197]
	s_mov_b32 m0, s8
	v_lshl_add_u64 v[222:223], v[222:223], 0, v[198:199]
	global_load_lds_dwordx4 v[224:225], off
	s_add_i32 m0, s8, 0x2000
	s_nop 0
	global_load_lds_dwordx4 v[222:223], off
	v_lshl_add_u64 v[222:223], v[244:245], 0, s[60:61]
	s_mov_b32 m0, s56
	s_nop 0
	global_load_lds_dwordx4 v[222:223], off
	v_lshl_add_u64 v[222:223], v[228:229], 0, s[60:61]
	s_mov_b32 m0, s57
	s_nop 0
	global_load_lds_dwordx4 v[222:223], off
	s_waitcnt vmcnt(8)
	s_waitcnt lgkmcnt(0)
	s_barrier
	s_setprio 1
	s_waitcnt lgkmcnt(0)
	v_mfma_f32_16x16x32_bf16 v[62:65], v[132:135], v[164:167], v[62:65]
	v_mfma_f32_16x16x32_bf16 v[54:57], v[140:143], v[164:167], v[54:57]
	v_mfma_f32_16x16x32_bf16 v[38:41], v[132:135], v[172:175], v[38:41]
	v_mfma_f32_16x16x32_bf16 v[34:37], v[140:143], v[172:175], v[34:37]
	v_mfma_f32_16x16x32_bf16 v[22:25], v[132:135], v[180:183], v[22:25]
	v_mfma_f32_16x16x32_bf16 v[18:21], v[140:143], v[180:183], v[18:21]
	v_mfma_f32_16x16x32_bf16 v[6:9], v[132:135], v[188:191], v[6:9]
	v_mfma_f32_16x16x32_bf16 v[2:5], v[140:143], v[188:191], v[2:5]
	v_mfma_f32_16x16x32_bf16 v[62:65], v[136:139], v[168:171], v[62:65]
	v_mfma_f32_16x16x32_bf16 v[54:57], v[144:147], v[168:171], v[54:57]
	v_mfma_f32_16x16x32_bf16 v[38:41], v[136:139], v[176:179], v[38:41]
	v_mfma_f32_16x16x32_bf16 v[34:37], v[144:147], v[176:179], v[34:37]
	v_mfma_f32_16x16x32_bf16 v[22:25], v[136:139], v[184:187], v[22:25]
	v_mfma_f32_16x16x32_bf16 v[18:21], v[144:147], v[184:187], v[18:21]
	v_mfma_f32_16x16x32_bf16 v[6:9], v[136:139], v[192:195], v[6:9]
	v_mfma_f32_16x16x32_bf16 v[2:5], v[144:147], v[192:195], v[2:5]
	s_setprio 0
	s_setprio 1
	v_mfma_f32_16x16x32_bf16 v[58:61], v[148:151], v[164:167], v[58:61]
	v_mfma_f32_16x16x32_bf16 v[50:53], v[156:159], v[164:167], v[50:53]
	v_mfma_f32_16x16x32_bf16 v[46:49], v[148:151], v[172:175], v[46:49]
	v_mfma_f32_16x16x32_bf16 v[42:45], v[156:159], v[172:175], v[42:45]
	v_mfma_f32_16x16x32_bf16 v[30:33], v[148:151], v[180:183], v[30:33]
	v_mfma_f32_16x16x32_bf16 v[26:29], v[156:159], v[180:183], v[26:29]
	v_mfma_f32_16x16x32_bf16 v[14:17], v[148:151], v[188:191], v[14:17]
	v_mfma_f32_16x16x32_bf16 v[10:13], v[156:159], v[188:191], v[10:13]
	v_mfma_f32_16x16x32_bf16 v[58:61], v[152:155], v[168:171], v[58:61]
	v_mfma_f32_16x16x32_bf16 v[50:53], v[160:163], v[168:171], v[50:53]
	v_mfma_f32_16x16x32_bf16 v[46:49], v[152:155], v[176:179], v[46:49]
	v_mfma_f32_16x16x32_bf16 v[42:45], v[160:163], v[176:179], v[42:45]
	v_mfma_f32_16x16x32_bf16 v[30:33], v[152:155], v[184:187], v[30:33]
	v_mfma_f32_16x16x32_bf16 v[26:29], v[160:163], v[184:187], v[26:29]
	v_mfma_f32_16x16x32_bf16 v[14:17], v[152:155], v[192:195], v[14:17]
	v_mfma_f32_16x16x32_bf16 v[10:13], v[160:163], v[192:195], v[10:13]
	s_setprio 0
	s_barrier
	s_add_i32 s45, s45, 2
	s_cmp_gt_u32 s45, 13
	s_mov_b64 s[36:37], s[84:85]
	s_cbranch_scc1 .LBB0_1247
	s_branch .LBB0_1239

.LBB0_1478:
	s_add_u32 s8, s74, 0x20080
	s_addc_u32 s9, s75, 0
	v_lshl_add_u64 v[214:215], s[8:9], 0, v[208:209]
	v_lshl_add_u64 v[216:217], s[8:9], 0, v[210:211]
	s_mov_b64 s[8:9], 0x100
	v_lshl_add_u64 v[218:219], v[2:3], 0, s[8:9]
	v_mov_b32_e32 v2, 0
	s_mov_b32 s8, -2
	s_mov_b64 s[84:85], 0
	s_xor_b64 s[86:87], s[36:37], -1
	v_add_u32_e32 v132, 0, v231
	v_add_u32_e32 v133, 0x10000, v132
	v_add_u32_e32 v144, 0x14000, v132
	ds_read_b128 v[148:151], v133
	ds_read_b128 v[152:155], v133 offset:1024
	ds_read_b128 v[156:159], v133 offset:2048
	ds_read_b128 v[160:163], v133 offset:3072
	ds_read_b128 v[132:135], v144
	ds_read_b128 v[136:139], v144 offset:1024
	ds_read_b128 v[140:143], v144 offset:2048
	ds_read_b128 v[144:147], v144 offset:3072
	s_cmp_lg_u32 s84, 0
	s_cselect_b64 s[10:11], -1, 0
	s_mov_b64 s[26:27], -1
	s_or_b64 s[40:41], s[86:87], s[10:11]
	v_lshl_add_u64 v[220:221], v[214:215], 0, s[84:85]
	s_add_i32 m0, s92, 0xc000
	ds_read_b128 v[188:191], v232
	ds_read_b128 v[192:195], v232 offset:1024
	ds_read_b128 v[180:183], v232 offset:2048
	ds_read_b128 v[184:187], v232 offset:3072
	ds_read_b128 v[172:175], v232 offset:4096
	ds_read_b128 v[176:179], v232 offset:5120
	ds_read_b128 v[164:167], v232 offset:6144
	ds_read_b128 v[168:171], v232 offset:7168
	global_load_lds_dwordx4 v[220:221], off
	v_lshl_add_u64 v[220:221], v[216:217], 0, s[84:85]
	s_add_i32 m0, s92, 0xe000
	s_and_b64 vcc, exec, s[40:41]
	global_load_lds_dwordx4 v[220:221], off
	s_cbranch_vccz .Lpeelg2_1482
	s_waitcnt vmcnt(8)
	s_mov_b64 s[26:27], 0

.Lpeelg2_1484:
	s_add_u32 s9, s74, s84
	s_addc_u32 s10, s75, s85
	s_add_u32 s9, s9, 0x100
	s_addc_u32 s10, s10, 0
	s_cmpk_eq_i32 s84, 0x300
	s_waitcnt lgkmcnt(0)
	v_lshl_add_u64 v[220:221], v[218:219], 0, s[84:85]
	s_cselect_b64 vcc, -1, 0
	s_cselect_b32 s37, s71, s10
	s_cselect_b32 s36, s70, s9
	v_cndmask_b32_e32 v221, v221, v213, vcc
	v_cndmask_b32_e32 v220, v220, v212, vcc
	s_barrier
	s_setprio 1
	s_waitcnt lgkmcnt(0)
	v_mfma_f32_16x16x32_bf16 v[128:131], v[148:151], v[188:191], 0
	v_mfma_f32_16x16x32_bf16 v[124:127], v[156:159], v[188:191], 0
	v_mfma_f32_16x16x32_bf16 v[116:119], v[148:151], v[180:183], 0
	v_mfma_f32_16x16x32_bf16 v[108:111], v[156:159], v[180:183], 0
	v_mfma_f32_16x16x32_bf16 v[100:103], v[148:151], v[172:175], 0
	v_mfma_f32_16x16x32_bf16 v[92:95], v[156:159], v[172:175], 0
	v_mfma_f32_16x16x32_bf16 v[84:87], v[148:151], v[164:167], 0
	v_mfma_f32_16x16x32_bf16 v[76:79], v[156:159], v[164:167], 0
	v_mfma_f32_16x16x32_bf16 v[128:131], v[152:155], v[192:195], v[128:131]
	v_mfma_f32_16x16x32_bf16 v[124:127], v[160:163], v[192:195], v[124:127]
	v_mfma_f32_16x16x32_bf16 v[116:119], v[152:155], v[184:187], v[116:119]
	v_mfma_f32_16x16x32_bf16 v[108:111], v[160:163], v[184:187], v[108:111]
	v_mfma_f32_16x16x32_bf16 v[100:103], v[152:155], v[176:179], v[100:103]
	v_mfma_f32_16x16x32_bf16 v[92:95], v[160:163], v[176:179], v[92:95]
	v_mfma_f32_16x16x32_bf16 v[84:87], v[152:155], v[168:171], v[84:87]
	v_mfma_f32_16x16x32_bf16 v[76:79], v[160:163], v[168:171], v[76:79]
	s_setprio 0
	s_setprio 1
	v_mfma_f32_16x16x32_bf16 v[120:123], v[132:135], v[188:191], 0
	v_mfma_f32_16x16x32_bf16 v[112:115], v[140:143], v[188:191], 0
	v_mfma_f32_16x16x32_bf16 v[104:107], v[132:135], v[180:183], 0
	v_mfma_f32_16x16x32_bf16 v[96:99], v[140:143], v[180:183], 0
	v_mfma_f32_16x16x32_bf16 v[88:91], v[132:135], v[172:175], 0
	v_mfma_f32_16x16x32_bf16 v[80:83], v[140:143], v[172:175], 0
	v_mfma_f32_16x16x32_bf16 v[72:75], v[132:135], v[164:167], 0
	v_mfma_f32_16x16x32_bf16 v[68:71], v[140:143], v[164:167], 0
	v_mfma_f32_16x16x32_bf16 v[120:123], v[136:139], v[192:195], v[120:123]
	v_mfma_f32_16x16x32_bf16 v[112:115], v[144:147], v[192:195], v[112:115]
	v_mfma_f32_16x16x32_bf16 v[104:107], v[136:139], v[184:187], v[104:107]
	v_mfma_f32_16x16x32_bf16 v[96:99], v[144:147], v[184:187], v[96:99]
	v_mfma_f32_16x16x32_bf16 v[88:91], v[136:139], v[176:179], v[88:91]
	v_mfma_f32_16x16x32_bf16 v[80:83], v[144:147], v[176:179], v[80:83]
	v_mfma_f32_16x16x32_bf16 v[72:75], v[136:139], v[168:171], v[72:75]
	v_mfma_f32_16x16x32_bf16 v[68:71], v[144:147], v[168:171], v[68:71]
	s_setprio 0
	s_barrier
	s_mov_b32 m0, s93
	v_lshl_add_u64 v[228:229], v[220:221], 0, v[198:199]
	ds_read_b128 v[188:191], v232 offset:16384
	ds_read_b128 v[192:195], v232 offset:17408
	ds_read_b128 v[180:183], v232 offset:18432
	ds_read_b128 v[184:187], v232 offset:19456
	ds_read_b128 v[172:175], v232 offset:20480
	ds_read_b128 v[176:179], v232 offset:21504
	ds_read_b128 v[164:167], v232 offset:22528
	ds_read_b128 v[168:171], v232 offset:23552
	global_load_lds_dwordx4 v[228:229], off
	v_lshl_add_u64 v[226:227], v[220:221], 0, v[202:203]
	s_mov_b32 m0, s94
	v_lshl_add_u64 v[222:223], v[220:221], 0, s[80:81]
	global_load_lds_dwordx4 v[226:227], off
	v_lshl_add_u64 v[224:225], v[222:223], 0, v[198:199]
	s_mov_b32 m0, s95
	v_lshl_add_u64 v[222:223], v[222:223], 0, v[202:203]
	global_load_lds_dwordx4 v[224:225], off
	s_mov_b32 m0, s96
	v_lshl_add_u64 v[224:225], s[36:37], 0, v[200:201]
	global_load_lds_dwordx4 v[222:223], off
	v_lshl_add_u64 v[222:223], s[36:37], 0, v[196:197]
	s_mov_b32 m0, s92
	s_mov_b64 s[26:27], -1
	global_load_lds_dwordx4 v[222:223], off
	s_mov_b32 m0, s97
	s_and_b64 vcc, exec, s[40:41]
	global_load_lds_dwordx4 v[224:225], off
	s_cbranch_vccz .Lpeelg2_1486
	s_waitcnt vmcnt(8)
	s_mov_b64 s[26:27], 0

.Lpeelg2_T:
	s_waitcnt lgkmcnt(0)
	s_barrier
	s_setprio 1
	s_waitcnt lgkmcnt(0)
	v_mfma_f32_16x16x32_bf16 v[62:65], v[148:151], v[188:191], 0
	v_mfma_f32_16x16x32_bf16 v[58:61], v[156:159], v[188:191], 0
	v_mfma_f32_16x16x32_bf16 v[50:53], v[148:151], v[180:183], 0
	v_mfma_f32_16x16x32_bf16 v[42:45], v[156:159], v[180:183], 0
	v_mfma_f32_16x16x32_bf16 v[34:37], v[148:151], v[172:175], 0
	v_mfma_f32_16x16x32_bf16 v[26:29], v[156:159], v[172:175], 0
	v_mfma_f32_16x16x32_bf16 v[18:21], v[148:151], v[164:167], 0
	v_mfma_f32_16x16x32_bf16 v[10:13], v[156:159], v[164:167], 0
	v_mfma_f32_16x16x32_bf16 v[62:65], v[152:155], v[192:195], v[62:65]
	v_mfma_f32_16x16x32_bf16 v[58:61], v[160:163], v[192:195], v[58:61]
	v_mfma_f32_16x16x32_bf16 v[50:53], v[152:155], v[184:187], v[50:53]
	v_mfma_f32_16x16x32_bf16 v[42:45], v[160:163], v[184:187], v[42:45]
	v_mfma_f32_16x16x32_bf16 v[34:37], v[152:155], v[176:179], v[34:37]
	v_mfma_f32_16x16x32_bf16 v[26:29], v[160:163], v[176:179], v[26:29]
	v_mfma_f32_16x16x32_bf16 v[18:21], v[152:155], v[168:171], v[18:21]
	v_mfma_f32_16x16x32_bf16 v[10:13], v[160:163], v[168:171], v[10:13]
	s_setprio 0
	s_setprio 1
	v_mfma_f32_16x16x32_bf16 v[54:57], v[132:135], v[188:191], 0
	v_mfma_f32_16x16x32_bf16 v[46:49], v[140:143], v[188:191], 0
	v_mfma_f32_16x16x32_bf16 v[38:41], v[132:135], v[180:183], 0
	v_mfma_f32_16x16x32_bf16 v[30:33], v[140:143], v[180:183], 0
	v_mfma_f32_16x16x32_bf16 v[22:25], v[132:135], v[172:175], 0
	v_mfma_f32_16x16x32_bf16 v[14:17], v[140:143], v[172:175], 0
	v_mfma_f32_16x16x32_bf16 v[6:9], v[132:135], v[164:167], 0
	v_mfma_f32_16x16x32_bf16 v[2:5], v[140:143], v[164:167], 0
	v_mfma_f32_16x16x32_bf16 v[54:57], v[136:139], v[192:195], v[54:57]
	v_mfma_f32_16x16x32_bf16 v[46:49], v[144:147], v[192:195], v[46:49]
	v_mfma_f32_16x16x32_bf16 v[38:41], v[136:139], v[184:187], v[38:41]
	v_mfma_f32_16x16x32_bf16 v[30:33], v[144:147], v[184:187], v[30:33]
	v_mfma_f32_16x16x32_bf16 v[22:25], v[136:139], v[176:179], v[22:25]
	v_mfma_f32_16x16x32_bf16 v[14:17], v[144:147], v[176:179], v[14:17]
	v_mfma_f32_16x16x32_bf16 v[6:9], v[136:139], v[168:171], v[6:9]
	v_mfma_f32_16x16x32_bf16 v[2:5], v[144:147], v[168:171], v[2:5]
	s_setprio 0
	s_barrier
	s_add_i32 s9, 0, 0x18000
	s_add_i32 s12, 0, 0x1c000
	v_add_u32_e32 v144, s9, v231
	v_add_u32_e32 v160, s12, v231
	ds_read_b128 v[132:135], v144
	ds_read_b128 v[136:139], v144 offset:1024
	ds_read_b128 v[140:143], v144 offset:2048
	ds_read_b128 v[144:147], v144 offset:3072
	ds_read_b128 v[148:151], v160
	ds_read_b128 v[152:155], v160 offset:1024
	ds_read_b128 v[156:159], v160 offset:2048
	ds_read_b128 v[160:163], v160 offset:3072
	s_add_u32 s10, s36, 0x20000
	s_addc_u32 s11, s37, 0
	s_mov_b32 m0, s50
	v_lshl_add_u64 v[234:235], s[10:11], 0, v[196:197]
	ds_read_b128 v[164:167], v232 offset:32768
	ds_read_b128 v[168:171], v232 offset:33792
	ds_read_b128 v[172:175], v232 offset:34816
	ds_read_b128 v[176:179], v232 offset:35840
	ds_read_b128 v[180:183], v232 offset:36864
	ds_read_b128 v[184:187], v232 offset:37888
	ds_read_b128 v[188:191], v232 offset:38912
	ds_read_b128 v[192:195], v232 offset:39936
	global_load_lds_dwordx4 v[234:235], off
	v_lshl_add_u64 v[234:235], s[10:11], 0, v[200:201]
	s_mov_b32 m0, s51
	s_nop 0
	global_load_lds_dwordx4 v[234:235], off
	s_waitcnt vmcnt(8)
	s_waitcnt lgkmcnt(0)
	s_barrier
	s_setprio 1
	s_waitcnt lgkmcnt(0)
	v_mfma_f32_16x16x32_bf16 v[128:131], v[132:135], v[164:167], v[128:131]
	v_mfma_f32_16x16x32_bf16 v[124:127], v[140:143], v[164:167], v[124:127]
	v_mfma_f32_16x16x32_bf16 v[116:119], v[132:135], v[172:175], v[116:119]
	v_mfma_f32_16x16x32_bf16 v[108:111], v[140:143], v[172:175], v[108:111]
	v_mfma_f32_16x16x32_bf16 v[100:103], v[132:135], v[180:183], v[100:103]
	v_mfma_f32_16x16x32_bf16 v[92:95], v[140:143], v[180:183], v[92:95]
	v_mfma_f32_16x16x32_bf16 v[84:87], v[132:135], v[188:191], v[84:87]
	v_mfma_f32_16x16x32_bf16 v[76:79], v[140:143], v[188:191], v[76:79]
	v_mfma_f32_16x16x32_bf16 v[128:131], v[136:139], v[168:171], v[128:131]
	v_mfma_f32_16x16x32_bf16 v[124:127], v[144:147], v[168:171], v[124:127]
	v_mfma_f32_16x16x32_bf16 v[116:119], v[136:139], v[176:179], v[116:119]
	v_mfma_f32_16x16x32_bf16 v[108:111], v[144:147], v[176:179], v[108:111]
	v_mfma_f32_16x16x32_bf16 v[100:103], v[136:139], v[184:187], v[100:103]
	v_mfma_f32_16x16x32_bf16 v[92:95], v[144:147], v[184:187], v[92:95]
	v_mfma_f32_16x16x32_bf16 v[84:87], v[136:139], v[192:195], v[84:87]
	v_mfma_f32_16x16x32_bf16 v[76:79], v[144:147], v[192:195], v[76:79]
	s_setprio 0
	s_setprio 1
	v_mfma_f32_16x16x32_bf16 v[120:123], v[148:151], v[164:167], v[120:123]
	v_mfma_f32_16x16x32_bf16 v[112:115], v[156:159], v[164:167], v[112:115]
	v_mfma_f32_16x16x32_bf16 v[104:107], v[148:151], v[172:175], v[104:107]
	v_mfma_f32_16x16x32_bf16 v[96:99], v[156:159], v[172:175], v[96:99]
	v_mfma_f32_16x16x32_bf16 v[88:91], v[148:151], v[180:183], v[88:91]
	v_mfma_f32_16x16x32_bf16 v[80:83], v[156:159], v[180:183], v[80:83]
	v_mfma_f32_16x16x32_bf16 v[72:75], v[148:151], v[188:191], v[72:75]
	v_mfma_f32_16x16x32_bf16 v[68:71], v[156:159], v[188:191], v[68:71]
	v_mfma_f32_16x16x32_bf16 v[120:123], v[152:155], v[168:171], v[120:123]
	v_mfma_f32_16x16x32_bf16 v[112:115], v[160:163], v[168:171], v[112:115]
	v_mfma_f32_16x16x32_bf16 v[104:107], v[152:155], v[176:179], v[104:107]
	v_mfma_f32_16x16x32_bf16 v[96:99], v[160:163], v[176:179], v[96:99]
	v_mfma_f32_16x16x32_bf16 v[88:91], v[152:155], v[184:187], v[88:91]
	v_mfma_f32_16x16x32_bf16 v[80:83], v[160:163], v[184:187], v[80:83]
	v_mfma_f32_16x16x32_bf16 v[72:75], v[152:155], v[192:195], v[72:75]
	v_mfma_f32_16x16x32_bf16 v[68:71], v[160:163], v[192:195], v[68:71]
	s_setprio 0
	s_barrier
	s_add_i32 s9, s9, s89
	v_lshl_add_u64 v[228:229], v[228:229], 0, s[60:61]
	s_mov_b32 m0, s9
	ds_read_b128 v[164:167], v232 offset:49152
	ds_read_b128 v[168:171], v232 offset:50176
	ds_read_b128 v[172:175], v232 offset:51200
	ds_read_b128 v[176:179], v232 offset:52224
	ds_read_b128 v[180:183], v232 offset:53248
	ds_read_b128 v[184:187], v232 offset:54272
	ds_read_b128 v[188:191], v232 offset:55296
	ds_read_b128 v[192:195], v232 offset:56320
	global_load_lds_dwordx4 v[228:229], off
	v_lshl_add_u64 v[226:227], v[226:227], 0, s[60:61]
	s_add_i32 m0, s9, 0x2000
	v_lshl_add_u64 v[220:221], v[220:221], 0, s[62:63]
	s_add_i32 s9, s12, s89
	global_load_lds_dwordx4 v[226:227], off
	v_lshl_add_u64 v[226:227], v[220:221], 0, v[198:199]
	s_mov_b32 m0, s9
	v_lshl_add_u64 v[220:221], v[220:221], 0, v[202:203]
	global_load_lds_dwordx4 v[226:227], off
	s_add_i32 m0, s9, 0x2000
	s_nop 0
	global_load_lds_dwordx4 v[220:221], off
	v_lshl_add_u64 v[220:221], v[222:223], 0, s[60:61]
	s_mov_b32 m0, s48
	s_nop 0
	global_load_lds_dwordx4 v[220:221], off
	v_lshl_add_u64 v[220:221], v[224:225], 0, s[60:61]
	s_mov_b32 m0, s49
	s_nop 0
	global_load_lds_dwordx4 v[220:221], off
	s_waitcnt vmcnt(8)
	s_waitcnt lgkmcnt(0)
	s_barrier
	s_setprio 1
	s_waitcnt lgkmcnt(0)
	v_mfma_f32_16x16x32_bf16 v[62:65], v[132:135], v[164:167], v[62:65]
	v_mfma_f32_16x16x32_bf16 v[58:61], v[140:143], v[164:167], v[58:61]
	v_mfma_f32_16x16x32_bf16 v[50:53], v[132:135], v[172:175], v[50:53]
	v_mfma_f32_16x16x32_bf16 v[42:45], v[140:143], v[172:175], v[42:45]
	v_mfma_f32_16x16x32_bf16 v[34:37], v[132:135], v[180:183], v[34:37]
	v_mfma_f32_16x16x32_bf16 v[26:29], v[140:143], v[180:183], v[26:29]
	v_mfma_f32_16x16x32_bf16 v[18:21], v[132:135], v[188:191], v[18:21]
	v_mfma_f32_16x16x32_bf16 v[10:13], v[140:143], v[188:191], v[10:13]
	v_mfma_f32_16x16x32_bf16 v[62:65], v[136:139], v[168:171], v[62:65]
	v_mfma_f32_16x16x32_bf16 v[58:61], v[144:147], v[168:171], v[58:61]
	v_mfma_f32_16x16x32_bf16 v[50:53], v[136:139], v[176:179], v[50:53]
	v_mfma_f32_16x16x32_bf16 v[42:45], v[144:147], v[176:179], v[42:45]
	v_mfma_f32_16x16x32_bf16 v[34:37], v[136:139], v[184:187], v[34:37]
	v_mfma_f32_16x16x32_bf16 v[26:29], v[144:147], v[184:187], v[26:29]
	v_mfma_f32_16x16x32_bf16 v[18:21], v[136:139], v[192:195], v[18:21]
	v_mfma_f32_16x16x32_bf16 v[10:13], v[144:147], v[192:195], v[10:13]
	s_setprio 0
	s_setprio 1
	v_mfma_f32_16x16x32_bf16 v[54:57], v[148:151], v[164:167], v[54:57]
	v_mfma_f32_16x16x32_bf16 v[46:49], v[156:159], v[164:167], v[46:49]
	v_mfma_f32_16x16x32_bf16 v[38:41], v[148:151], v[172:175], v[38:41]
	v_mfma_f32_16x16x32_bf16 v[30:33], v[156:159], v[172:175], v[30:33]
	v_mfma_f32_16x16x32_bf16 v[22:25], v[148:151], v[180:183], v[22:25]
	v_mfma_f32_16x16x32_bf16 v[14:17], v[156:159], v[180:183], v[14:17]
	v_mfma_f32_16x16x32_bf16 v[6:9], v[148:151], v[188:191], v[6:9]
	v_mfma_f32_16x16x32_bf16 v[2:5], v[156:159], v[188:191], v[2:5]
	v_mfma_f32_16x16x32_bf16 v[54:57], v[152:155], v[168:171], v[54:57]
	v_mfma_f32_16x16x32_bf16 v[46:49], v[160:163], v[168:171], v[46:49]
	v_mfma_f32_16x16x32_bf16 v[38:41], v[152:155], v[176:179], v[38:41]
	v_mfma_f32_16x16x32_bf16 v[30:33], v[160:163], v[176:179], v[30:33]
	v_mfma_f32_16x16x32_bf16 v[22:25], v[152:155], v[184:187], v[22:25]
	v_mfma_f32_16x16x32_bf16 v[14:17], v[160:163], v[184:187], v[14:17]
	v_mfma_f32_16x16x32_bf16 v[6:9], v[152:155], v[192:195], v[6:9]
	v_mfma_f32_16x16x32_bf16 v[2:5], v[160:163], v[192:195], v[2:5]
	s_setprio 0
	s_barrier
	s_add_i32 s8, s8, 2
	s_add_u32 s84, s84, 0x100
	s_addc_u32 s85, s85, 0
	s_cmp_gt_u32 s8, 5
	s_cbranch_scc1 .LBB0_1488
	s_branch .LBB0_1480
